# speedup vs baseline: 1.0149x; 1.0149x over previous
.LBB2_52:
	v_min_i32_e32 v2, v27, v49
	v_lshlrev_b32_e32 v2, 3, v2
	v_add_u32_e32 v54, 1, v27
	ds_read_b64 v[38:39], v2 offset:8704
	v_min_i32_e32 v2, v54, v49
	v_add_u32_e32 v52, 2, v27
	v_add_u32_e32 v50, 3, v27
	v_lshlrev_b32_e32 v2, 3, v2
	v_min_i32_e32 v3, v52, v49
	v_min_i32_e32 v4, v50, v49
	v_lshlrev_b32_e32 v3, 3, v3
	v_lshlrev_b32_e32 v4, 3, v4
	ds_read_b64 v[34:35], v2 offset:8704
	ds_read_b64 v[30:31], v3 offset:8704
	ds_read_b64 v[28:29], v4 offset:8704
	s_waitcnt lgkmcnt(0)
	v_lshlrev_b32_sdwa v41, v47, v38 dst_sel:DWORD dst_unused:UNUSED_PAD src0_sel:DWORD src1_sel:WORD_0
	v_lshlrev_b32_sdwa v51, v47, v34 dst_sel:DWORD dst_unused:UNUSED_PAD src0_sel:DWORD src1_sel:WORD_0
	v_lshlrev_b32_sdwa v53, v47, v30 dst_sel:DWORD dst_unused:UNUSED_PAD src0_sel:DWORD src1_sel:WORD_0
	v_lshlrev_b32_sdwa v57, v47, v28 dst_sel:DWORD dst_unused:UNUSED_PAD src0_sel:DWORD src1_sel:WORD_0
	global_load_dword v56, v41, s[44:45]
	global_load_dword v55, v51, s[44:45]
	global_load_dword v53, v53, s[44:45]
	global_load_dword v51, v57, s[44:45]
	v_lshlrev_b32_e32 v2, 4, v38
	v_lshlrev_b32_e32 v3, 4, v34
	v_and_or_b32 v2, v2, s67, v1
	v_and_or_b32 v3, v3, s67, v1
	v_lshlrev_b32_e32 v2, 4, v2
	v_lshlrev_b32_e32 v3, 4, v3
	global_load_dwordx4 v[14:17], v2, s[36:37]
	global_load_dwordx4 v[10:13], v3, s[36:37]
	v_lshlrev_b32_e32 v2, 4, v30
	v_lshlrev_b32_e32 v3, 4, v28
	v_and_or_b32 v2, v2, s67, v1
	v_and_or_b32 v3, v3, s67, v1
	v_lshlrev_b32_e32 v2, 4, v2
	v_lshlrev_b32_e32 v3, 4, v3
	global_load_dwordx4 v[6:9], v2, s[36:37]
	s_nop 0
	global_load_dwordx4 v[2:5], v3, s[36:37]
	v_bfe_u32 v38, v38, 16, 4
	v_cmp_ne_u32_e64 s[34:35], v38, v40
	s_and_saveexec_b64 s[60:61], s[34:35]
	s_cbranch_execz .LBB2_62
	v_cmp_lt_i32_e64 s[34:35], -1, v40
	s_mov_b64 s[64:65], s[56:57]
	s_and_saveexec_b64 s[62:63], s[34:35]
	s_cbranch_execz .LBB2_61
	s_xor_b64 s[34:35], s[56:57], -1
	s_and_saveexec_b64 s[64:65], s[34:35]
	s_xor_b64 s[34:35], exec, s[64:65]
	s_cbranch_execz .LBB2_56
	v_mad_u64_u32 v[40:41], s[64:65], v40, s66, v[24:25]
	ds_read_b128 v[58:61], v40
	s_waitcnt lgkmcnt(0)
	v_cvt_f32_f16_e32 v62, v58
	v_cvt_f32_f16_sdwa v63, v58 dst_sel:DWORD dst_unused:UNUSED_PAD src0_sel:WORD_1
	v_cvt_f32_f16_e32 v58, v59
	v_cvt_f32_f16_sdwa v59, v59 dst_sel:DWORD dst_unused:UNUSED_PAD src0_sel:WORD_1
	v_pk_add_f32 v[18:19], v[18:19], v[62:63]
	s_nop 0
	v_cvt_pk_f16_f32 v18, v18, v19
	v_pk_add_f32 v[36:37], v[36:37], v[58:59]
	s_nop 0
	v_cvt_pk_f16_f32 v19, v36, v37
	v_cvt_f32_f16_e32 v36, v60
	v_cvt_f32_f16_sdwa v37, v60 dst_sel:DWORD dst_unused:UNUSED_PAD src0_sel:WORD_1
	v_pk_add_f32 v[20:21], v[20:21], v[36:37]
	v_cvt_f32_f16_e32 v36, v61
	v_cvt_f32_f16_sdwa v37, v61 dst_sel:DWORD dst_unused:UNUSED_PAD src0_sel:WORD_1
	v_cvt_pk_f16_f32 v20, v20, v21
	v_pk_add_f32 v[32:33], v[32:33], v[36:37]
	s_nop 0
	v_cvt_pk_f16_f32 v21, v32, v33
	ds_write_b128 v40, v[18:21]

.LBB2_62:
	s_or_b64 exec, exec, s[60:61]
	s_waitcnt vmcnt(0)
	v_mul_f32_e32 v38, v39, v56
	v_cvt_f32_f16_sdwa v57, v14 dst_sel:DWORD dst_unused:UNUSED_PAD src0_sel:WORD_1
	v_cvt_f32_f16_e32 v56, v14
	v_cvt_f32_f16_sdwa v59, v15 dst_sel:DWORD dst_unused:UNUSED_PAD src0_sel:WORD_1
	v_cvt_f32_f16_e32 v58, v15
	v_cvt_f32_f16_sdwa v15, v16 dst_sel:DWORD dst_unused:UNUSED_PAD src0_sel:WORD_1
	v_cvt_f32_f16_e32 v14, v16
	v_cvt_f32_f16_sdwa v61, v17 dst_sel:DWORD dst_unused:UNUSED_PAD src0_sel:WORD_1
	v_cvt_f32_f16_e32 v60, v17
	v_pk_fma_f32 v[18:19], v[38:39], v[56:57], v[18:19] op_sel_hi:[0,1,1]
	v_pk_fma_f32 v[16:17], v[38:39], v[14:15], v[20:21] op_sel_hi:[0,1,1]
	v_bfe_u32 v20, v34, 16, 4
	v_pk_fma_f32 v[36:37], v[38:39], v[58:59], v[36:37] op_sel_hi:[0,1,1]
	v_pk_fma_f32 v[14:15], v[38:39], v[60:61], v[32:33] op_sel_hi:[0,1,1]
	v_cmp_ne_u32_e64 s[34:35], v20, v40
	s_and_saveexec_b64 s[60:61], s[34:35]
	s_cbranch_execz .LBB2_70
	s_xor_b64 s[34:35], s[56:57], -1
	s_and_saveexec_b64 s[62:63], s[34:35]
	s_xor_b64 s[34:35], exec, s[62:63]
	s_cbranch_execz .LBB2_65
	v_mad_u64_u32 v[32:33], s[62:63], v40, s66, v[24:25]
	ds_read_b128 v[38:41], v32
	s_waitcnt lgkmcnt(0)
	v_cvt_f32_f16_e32 v56, v38
	v_cvt_f32_f16_sdwa v57, v38 dst_sel:DWORD dst_unused:UNUSED_PAD src0_sel:WORD_1
	v_cvt_f32_f16_e32 v38, v39
	v_cvt_f32_f16_sdwa v39, v39 dst_sel:DWORD dst_unused:UNUSED_PAD src0_sel:WORD_1
	v_cvt_f32_f16_e32 v58, v40
	v_pk_add_f32 v[18:19], v[18:19], v[56:57]
	v_cvt_f32_f16_sdwa v59, v40 dst_sel:DWORD dst_unused:UNUSED_PAD src0_sel:WORD_1
	v_pk_add_f32 v[38:39], v[36:37], v[38:39]
	v_cvt_pk_f16_f32 v36, v18, v19
	v_cvt_f32_f16_e32 v18, v41
	v_cvt_f32_f16_sdwa v19, v41 dst_sel:DWORD dst_unused:UNUSED_PAD src0_sel:WORD_1
	v_pk_add_f32 v[16:17], v[16:17], v[58:59]
	v_cvt_pk_f16_f32 v37, v38, v39
	v_cvt_pk_f16_f32 v38, v16, v17
	v_pk_add_f32 v[14:15], v[14:15], v[18:19]
	s_nop 0
	v_cvt_pk_f16_f32 v39, v14, v15
	ds_write_b128 v32, v[36:39]
